# static s_setprio 1 for waves 4-7 during the attention phase (NSA+DSA), reset to 0 at phase end
# baseline (speedup 1.0000x reference)
.LBB0_593:
	v_readlane_b32 s4, v254, 4
	v_readlane_b32 s6, v254, 6
	s_cmp_le_i32 s6, s18
	s_cselect_b64 s[0:1], -1, 0
	v_readlane_b32 s5, v254, 5
	v_readlane_b32 s7, v254, 7
	v_writelane_b32 v254, s0, 26
	s_nop 1
	v_writelane_b32 v254, s1, 27
	s_and_b64 s[0:1], s[0:1], s[2:3]
	s_andn2_b64 vcc, exec, s[0:1]
	s_cbranch_vccnz .LBB0_2615
	v_readlane_b32 s0, v250, 56
	v_mov_b32_e32 v152, v0
	v_readlane_b32 s1, v250, 57
	s_load_dword s0, s[0:1], 0x0
	v_readfirstlane_b32 s21, v152
	s_cmpk_ge_u32 s21, 0x100
	s_cbranch_scc0 .Lprio5_done
	s_setprio 1
.Lprio5_done:
	s_waitcnt lgkmcnt(0)
	v_writelane_b32 v254, s0, 28
	s_and_b32 s0, s0, 7
	s_cmp_lg_u32 s0, 0
	v_readlane_b32 s0, v253, 31
	s_mov_b32 s20, s0
	v_readlane_b32 s1, v253, 32
	s_cbranch_scc0 .LBB0_596
	s_movk_i32 s0, 0x2000
	v_cmp_gt_i32_e32 vcc, s0, v152
	s_and_saveexec_b64 s[0:1], vcc
	s_cbranch_execnz .LBB0_597
	s_branch .LBB0_601

.LBB0_2615:
	s_setprio 0
	v_readlane_b32 s0, v254, 25
	s_or_b32 s18, s0, 6
	v_readlane_b32 s0, v254, 4
	v_readlane_b32 s1, v254, 5
	v_readlane_b32 s3, v254, 7
	v_readlane_b32 s2, v254, 6
	s_cmp_lt_i32 s18, s3
	v_readlane_b32 s0, v254, 26
	s_cselect_b64 s[2:3], -1, 0
	v_readlane_b32 s1, v254, 27
	s_and_b64 s[0:1], s[0:1], s[2:3]
	s_andn2_b64 vcc, exec, s[0:1]
	s_cbranch_vccnz .LBB0_2665
	s_waitcnt vmcnt(0)
	s_waitcnt vmcnt(0) lgkmcnt(0)
	s_barrier
	s_mov_b64 s[0:1], exec
	v_readlane_b32 s4, v254, 19
	v_readlane_b32 s5, v254, 20
	s_and_b64 s[4:5], s[0:1], s[4:5]
	s_mov_b64 exec, s[4:5]
	s_cbranch_execz .LBB0_2664
	v_readlane_b32 s4, v254, 10
	s_waitcnt vmcnt(0) expcnt(0) lgkmcnt(0)
	s_nop 0
	v_mov_b32_e32 v1, s4
	ds_read_b32 v7, v1
	v_readlane_b32 s4, v254, 11
	s_waitcnt lgkmcnt(0)
	v_cmp_ne_u32_e32 vcc, 0, v7
	v_mov_b32_e32 v1, s4
	ds_read_b32 v6, v1
	s_cbranch_vccnz .LBB0_2632
	v_readlane_b32 s6, v250, 56
	v_readlane_b32 s7, v250, 57
	s_load_dwordx2 s[4:5], s[6:7], 0x0
	s_nop 0
	s_load_dword s6, s[6:7], 0x8
	s_mov_b32 s11, 1
	s_waitcnt lgkmcnt(0)
	s_mul_i32 s10, s5, s4
	s_mul_i32 s10, s10, s6
	s_branch .LBB0_2620
